# final phase: each wave touches its four x1 rows before waiting for the grid barrier, so workgroups that arrive early pull them into cache while HBM is lightly used
# speedup vs baseline: 1.0008x; 1.0001x over previous
; #define GAS __attribute__((address_space(1)))
; __device__ __forceinline__ int lane_id_v() { int l; asm volatile("v_mbcnt_lo_u32_b32 %0, -1, 0\n\tv_mbcnt_hi_u32_b32 %0, -1, %0" : "=v"(l)); return l; }
; __global__ void __launch_bounds__(512, 2) hymba_fwd(Args args) {
;     ...
;             const int lane = lane_id_v();
;             const int* tokpos = (const int*)(ws + WS_TOKPOS);
;             for (int tq = gw; tq < SEQ; tq += 4 * NGW) {
;             int cc0[4], cc1[4];
; #pragma unroll
;             for (int k = 0; k < 4; ++k) { const int t = tq + k * NGW; cc0[k] = 0; cc1[k] = 0; if (t < SEQ) { cc0[k] = tokpos[2 * t]; cc1[k] = tokpos[2 * t + 1]; } }
;             v2u xb[2][8]; unsigned b0[2][8], b1[2][8];
;             auto ld = [&](int k) { const int t = tq + k * NGW; const int c0 = cc0[k], c1 = cc1[k];
;                 const size_t r0 = (size_t)(256 * tb[c0 >> 16] + (c0 & 0xffff)), r1 = (size_t)(256 * tb[c1 >> 16] + (c1 & 0xffff));
;                 const GAS v2u* xo = (const GAS v2u*)(X1B + (size_t)t * DM) + lane; const GAS unsigned* y0 = (const GAS unsigned*)((const unsigned char*)Yb + r0 * DM) + lane; const GAS unsigned* y1 = (const GAS unsigned*)((const unsigned char*)Yb + r1 * DM) + lane;
; #pragma unroll
;                 for (int j = 0; j < 8; ++j) { xb[k & 1][j] = __builtin_nontemporal_load(xo + 64 * j); b0[k & 1][j] = __builtin_nontemporal_load(y0 + 64 * j); b1[k & 1][j] = __builtin_nontemporal_load(y1 + 64 * j); } };
.LBB0_909:
	s_mov_b32 s98, 0
	s_cmp_lt_i32 s94, 8
	s_cselect_b64 s[0:1], -1, 0
	s_cmp_gt_i32 s95, 7
	s_cselect_b64 s[6:7], -1, 0
	s_and_b64 s[0:1], s[0:1], s[6:7]
	s_andn2_b64 vcc, exec, s[0:1]
	s_cbranch_vccnz .LBB0_929
	s_cmpk_gt_i32 s34, 0x1fff
	s_waitcnt vmcnt(0)
	v_mbcnt_lo_u32_b32 v8, -1, 0
	v_mbcnt_hi_u32_b32 v8, -1, v8
	s_cbranch_scc1 .LBB0_929
	s_lshl_b32 s99, s34, 12
	s_add_u32 s100, s26, 0x5000000
	s_addc_u32 s101, s27, 0
	s_add_u32 s100, s100, s99
	s_addc_u32 s101, s101, 0
	v_mbcnt_lo_u32_b32 v110, -1, 0
	v_mbcnt_hi_u32_b32 v110, -1, v110
	v_lshrrev_b32_e32 v111, 5, v110
	v_and_b32_e32 v110, 31, v110
	v_lshlrev_b32_e32 v110, 7, v110
	v_lshl_or_b32 v110, v111, 23, v110
	global_load_dword v111, v110, s[100:101]
	s_add_u32 s100, s100, 0x1000000
	s_addc_u32 s101, s101, 0
	global_load_dword v111, v110, s[100:101]
	s_add_u32 s19, s26, 0x300000
	s_addc_u32 s30, s27, 0
	s_lshl_b32 s0, s2, 4
	s_lshl_b32 s1, s92, 1
	s_add_i32 s2, s0, s1
	s_add_i32 s0, s34, s90
	v_ashrrev_i32_e32 v9, 31, v8
	s_ashr_i32 s1, s0, 31
	v_lshlrev_b64 v[0:1], 4, v[8:9]
	s_lshl_b32 s6, s3, 5
	v_lshlrev_b64 v[4:5], 3, v[8:9]
	v_lshl_add_u64 v[8:9], v[8:9], 2, s[4:5]
	s_lshl_b32 s31, s3, 6
	s_lshl_b32 s33, s3, 4
	s_lshl_b64 s[4:5], s[0:1], 13
	s_add_u32 s4, s24, s4
	s_addc_u32 s5, s25, s5
	s_ashr_i32 s7, s6, 31
	s_ashr_i32 s35, s34, 31
	s_lshl_b64 s[8:9], s[6:7], 13
	s_lshl_b64 s[10:11], s[34:35], 12
	s_add_u32 s10, s26, s10
	s_addc_u32 s11, s27, s11
	s_lshl_b64 s[12:13], s[6:7], 12
	s_lshl_b64 s[0:1], s[0:1], 12
	s_add_u32 s14, s26, s0
	s_addc_u32 s15, s27, s1
	s_lshl_b64 s[0:1], s[34:35], 13
	s_add_u32 s16, s24, s0
	v_lshl_add_u64 v[2:3], s[24:25], 0, v[0:1]
	v_lshl_add_u64 v[6:7], s[38:39], 0, v[4:5]
	s_mul_i32 s36, s3, 24
	s_mul_i32 s37, s3, 48
	s_addc_u32 s17, s25, s1
	v_mov_b32_e32 v48, 0
	s_add_i32 s7, 0, 0x22400
	s_mov_b32 s35, 0x5000000
	s_mov_b32 s18, 0x3d800000
	s_movk_i32 s38, 0x1000
	v_mov_b32_e32 v49, 2
	s_branch .LBB0_913
